# fuse MoE dispatch gather into P8 A-operand LDS-DMA: P7 builds slot->token table only (no XS row copies), P8 A tiles read U2 rows via per-lane token offsets, pad slots -> zero row
# speedup vs baseline: 1.0175x; 1.0175x over previous
.LBB0_1112:
	s_or_b64 exec, exec, s[0:1]
	s_mov_b32 s10, s86
	s_waitcnt lgkmcnt(0)
	s_barrier
	v_lshl_add_u32 v0, s86, 6, v213
	s_add_u32 s26, s6, 0x2b500000
	s_addc_u32 s27, s7, 0
	v_readlane_b32 s0, v252, 6
	v_readlane_b32 s1, v252, 7
	s_nop 0
	s_andn2_b64 vcc, exec, s[0:1]
	s_cbranch_vccnz .Lgat_nopad
	v_readlane_b32 s0, v252, 9
	v_readlane_b32 s1, v252, 10
	s_nop 0
	v_mov_b32_e32 v2, s0
	ds_read2_b32 v[2:3], v2 offset1:1
	v_mov_b32_e32 v4, s1
	ds_read_b32 v4, v4
	v_mov_b32_e32 v5, 0x10800
	s_waitcnt lgkmcnt(0)
	v_add3_u32 v2, v2, v4, v0
	s_mov_b64 s[28:29], exec
.Lgat_padloop:
	v_cmp_lt_i32_e32 vcc, v2, v3
	s_and_b64 exec, exec, vcc
	s_cbranch_execz .Lgat_padend
	v_lshlrev_b32_e32 v4, 2, v2
	global_store_dword v4, v5, s[26:27]
	v_add_u32_e32 v2, 0x200, v2
	s_branch .Lgat_padloop
.Lgat_padend:
	s_mov_b64 exec, s[28:29]
.Lgat_nopad:
	s_cmpk_lg_u32 s82, 40
	s_cbranch_scc1 .Lgat_nozero
	s_cmp_lg_u32 s86, 0
	s_cbranch_scc1 .Lgat_nozero
	s_add_u32 s0, s6, 0x16b00000
	s_addc_u32 s1, s7, 0
	v_lshlrev_b32_e32 v2, 4, v213
	global_store_dwordx4 v2, v[242:245], s[0:1]
.Lgat_nozero:
	s_lshr_b32 s14, s46, 4
	s_mul_i32 s0, s86, s83
	s_add_i32 s37, s82, s0
	s_lshl_b32 s23, s83, 3
	s_cmp_ge_i32 s37, s14
	s_cbranch_scc1 .Lgat_done
	s_add_u32 s30, s6, 0x300000
	s_addc_u32 s31, s7, 0
	s_add_u32 s32, s6, 0x500000
	s_addc_u32 s33, s7, 0
	s_add_u32 s34, s6, 0x900000
	s_addc_u32 s35, s7, 0
.Lgat_loop:
	v_lshl_add_u32 v2, s37, 6, v213
	v_lshlrev_b32_e32 v3, 2, v2
	global_load_dword v4, v3, s[30:31]
	global_load_dword v5, v3, s[32:33]
	v_lshrrev_b32_e32 v8, 2, v2
	s_waitcnt vmcnt(1)
	v_lshlrev_b32_e32 v6, 2, v4
	v_add_u32_e32 v7, 0x200c0, v6
	v_add_u32_e32 v6, 0x20150, v6
	ds_read_b32 v7, v7
	ds_read_b32 v6, v6
	s_waitcnt vmcnt(0) lgkmcnt(0)
	v_add3_u32 v5, v7, v6, v5
	v_lshlrev_b32_e32 v9, 2, v5
	global_store_dword v3, v5, s[34:35]
	global_store_dword v9, v8, s[26:27]
	s_add_i32 s37, s37, s23
	s_cmp_lt_i32 s37, s14
	s_cbranch_scc1 .Lgat_loop
.Lgat_done:
.LBB0_1135:
	v_readlane_b32 s24, v253, 45
	v_readlane_b32 s25, v253, 46

.LBB0_1217:
	v_readlane_b32 s0, v253, 9
	s_nop 1
	v_mov_b32_e32 v0, s0
	ds_read_b32 v2, v0
	s_mov_b32 s0, s86
	s_waitcnt lgkmcnt(0)
	v_readfirstlane_b32 s38, v2
	v_lshl_add_u32 v0, s0, 6, v213
	v_readlane_b32 s0, v252, 13
	s_cmp_ge_i32 s0, s38
	v_readfirstlane_b32 s14, v0
	v_readlane_b32 s1, v252, 14
	s_cbranch_scc1 .LBB0_1233
	v_bfe_i32 v4, v0, 27, 1
	v_lshlrev_b32_e32 v2, 4, v0
	v_lshrrev_b32_e32 v4, 22, v4
	v_add_u32_e32 v4, v2, v4
	v_and_b32_e32 v4, 0xfffffc00, v4
	v_sub_u32_e32 v4, v2, v4
	v_ashrrev_i32_e32 v3, 31, v0
	v_lshrrev_b32_e32 v5, 4, v4
	s_mov_b32 s57, s15
	v_lshrrev_b32_e32 v3, 26, v3
	v_bitop3_b32 v5, v5, v4, 32 bitop3:0x6c
	v_ashrrev_i32_e32 v4, 31, v4
	s_lshl_b64 s[0:1], s[56:57], 26
	v_add_u32_e32 v3, v0, v3
	v_lshrrev_b32_e32 v4, 26, v4
	s_add_u32 s39, s10, 0x12900000
	v_ashrrev_i32_e32 v3, 6, v3
	v_add_u32_e32 v4, v5, v4
	s_addc_u32 s40, s11, 0
	v_lshlrev_b32_e32 v6, 3, v3
	v_ashrrev_i32_e32 v4, 6, v4
	s_add_u32 s0, s10, s0
	v_and_b32_e32 v6, -16, v6
	v_mul_i32_i24_e32 v7, 64, v4
	s_addc_u32 s1, s11, s1
	v_add_u32_e32 v6, v4, v6
	v_sub_u32_e32 v5, v5, v7
	s_add_u32 s41, s0, 0x6900000
	v_lshlrev_b32_e32 v3, 5, v3
	v_ashrrev_i16_sdwa v5, v210, sext(v5) dst_sel:DWORD dst_unused:UNUSED_PAD src0_sel:DWORD src1_sel:BYTE_0
	v_lshlrev_b32_e32 v7, 1, v6
	v_lshrrev_b32_e32 v8, 2, v6
	v_and_b32_e32 v4, 3, v4
	s_mov_b32 s0, 0x3fffe0
	v_and_b32_e32 v3, 32, v3
	v_bfe_i32 v5, v5, 0, 16
	v_and_b32_e32 v7, 24, v7
	v_and_b32_e32 v8, 4, v8
	v_and_or_b32 v4, v6, s0, v4
	v_or3_b32 v4, v4, v8, v7
	v_add_lshl_u32 v3, v3, v5, 1
	v_add_u32_e32 v2, 0x2000, v2
	s_waitcnt vmcnt(0)
	v_lshl_add_u32 v164, v6, 10, v3
	v_mov_b32_e32 v234, v3
	v_lshlrev_b32_e32 v236, 2, v6
	v_lshl_add_u32 v165, v4, 10, v3
	v_ashrrev_i32_e32 v3, 31, v2
	v_lshrrev_b32_e32 v3, 22, v3
	v_add_u32_e32 v3, v2, v3
	v_ashrrev_i32_e32 v3, 10, v3
	v_mul_i32_i24_e32 v4, 0x400, v3
	v_sub_u32_e32 v2, v2, v4
	v_lshrrev_b32_e32 v4, 4, v2
	v_bitop3_b32 v2, v4, v2, 32 bitop3:0x6c
	v_ashrrev_i32_e32 v5, 31, v2
	v_lshrrev_b32_e32 v5, 26, v5
	v_lshlrev_b32_e32 v4, 3, v3
	v_add_u32_e32 v5, v2, v5
	v_and_b32_e32 v4, -16, v4
	v_ashrrev_i32_e32 v6, 6, v5
	v_and_b32_e32 v5, 0xc0, v5
	v_add_u32_e32 v4, v6, v4
	v_sub_u32_e32 v2, v2, v5
	v_lshlrev_b32_e32 v3, 5, v3
	v_ashrrev_i16_sdwa v2, v210, sext(v2) dst_sel:DWORD dst_unused:UNUSED_PAD src0_sel:DWORD src1_sel:BYTE_0
	v_lshlrev_b32_e32 v5, 1, v4
	v_lshrrev_b32_e32 v7, 2, v4
	v_and_b32_e32 v6, 3, v6
	v_and_b32_e32 v3, 32, v3
	v_bfe_i32 v2, v2, 0, 16
	v_and_b32_e32 v5, 24, v5
	v_and_b32_e32 v7, 4, v7
	v_and_or_b32 v6, v4, s0, v6
	v_or3_b32 v5, v6, v7, v5
	v_add_lshl_u32 v2, v3, v2, 1
	v_readlane_b32 s0, v252, 12
	v_lshl_add_u32 v166, v4, 10, v2
	v_mov_b32_e32 v235, v2
	v_lshlrev_b32_e32 v237, 2, v4
	v_lshl_add_u32 v167, v5, 10, v2
	v_mov_b32_e32 v2, s0
	ds_read_u16 v2, v2
	s_addc_u32 s42, s1, 0
	v_readlane_b32 s1, v252, 11
	s_ashr_i32 s17, s14, 6
	v_readlane_b32 s20, v253, 4
	s_waitcnt lgkmcnt(0)
	v_readfirstlane_b32 s0, v2
	s_and_b32 s0, s0, 0xffff
	s_lshl_b32 s0, s0, 3
	s_add_i32 s24, s0, s1
	s_ashr_i32 s25, s24, 31
	s_ashr_i32 s16, s14, 8
	s_lshl_b32 s8, s17, 10
	v_readlane_b32 s22, v253, 6
	v_readlane_b32 s23, v253, 7
	s_lshl_b64 s[0:1], s[24:25], 18
	v_readlane_b32 s21, v253, 5
	v_mov_b64_e32 v[36:37], s[22:23]
	v_mov_b64_e32 v[156:157], s[22:23]
	v_mov_b64_e32 v[148:149], s[22:23]
	v_mov_b64_e32 v[140:141], s[22:23]
	v_mov_b64_e32 v[132:133], s[22:23]
	v_mov_b64_e32 v[124:125], s[22:23]
	v_mov_b64_e32 v[116:117], s[22:23]
	v_mov_b64_e32 v[108:109], s[22:23]
	v_mov_b64_e32 v[100:101], s[22:23]
	v_mov_b64_e32 v[160:161], s[22:23]
	v_mov_b64_e32 v[152:153], s[22:23]
	v_mov_b64_e32 v[144:145], s[22:23]
	v_mov_b64_e32 v[136:137], s[22:23]
	v_mov_b64_e32 v[128:129], s[22:23]
	v_mov_b64_e32 v[120:121], s[22:23]
	v_mov_b64_e32 v[112:113], s[22:23]
	v_mov_b64_e32 v[104:105], s[22:23]
	v_mov_b64_e32 v[92:93], s[22:23]
	v_mov_b64_e32 v[84:85], s[22:23]
	v_mov_b64_e32 v[76:77], s[22:23]
	v_mov_b64_e32 v[68:69], s[22:23]
	v_mov_b64_e32 v[60:61], s[22:23]
	v_mov_b64_e32 v[52:53], s[22:23]
	v_mov_b64_e32 v[44:45], s[22:23]
	v_mov_b64_e32 v[40:41], s[22:23]
	v_mov_b64_e32 v[96:97], s[22:23]
	v_mov_b64_e32 v[88:89], s[22:23]
	v_mov_b64_e32 v[80:81], s[22:23]
	v_mov_b64_e32 v[72:73], s[22:23]
	v_mov_b64_e32 v[64:65], s[22:23]
	v_mov_b64_e32 v[56:57], s[22:23]
	v_mov_b64_e32 v[48:49], s[22:23]
	s_add_u32 s26, s41, s0
	v_mov_b64_e32 v[34:35], s[20:21]
	v_mov_b64_e32 v[154:155], s[20:21]
	v_mov_b64_e32 v[146:147], s[20:21]
	v_mov_b64_e32 v[138:139], s[20:21]
	v_mov_b64_e32 v[130:131], s[20:21]
	v_mov_b64_e32 v[122:123], s[20:21]
	v_mov_b64_e32 v[114:115], s[20:21]
	v_mov_b64_e32 v[106:107], s[20:21]
	v_mov_b64_e32 v[98:99], s[20:21]
	v_mov_b64_e32 v[158:159], s[20:21]
	v_mov_b64_e32 v[150:151], s[20:21]
	v_mov_b64_e32 v[142:143], s[20:21]
	v_mov_b64_e32 v[134:135], s[20:21]
	v_mov_b64_e32 v[126:127], s[20:21]
	v_mov_b64_e32 v[118:119], s[20:21]
	v_mov_b64_e32 v[110:111], s[20:21]
	v_mov_b64_e32 v[102:103], s[20:21]
	v_mov_b64_e32 v[90:91], s[20:21]
	v_mov_b64_e32 v[82:83], s[20:21]
	v_mov_b64_e32 v[74:75], s[20:21]
	v_mov_b64_e32 v[66:67], s[20:21]
	v_mov_b64_e32 v[58:59], s[20:21]
	v_mov_b64_e32 v[50:51], s[20:21]
	v_mov_b64_e32 v[42:43], s[20:21]
	v_mov_b64_e32 v[38:39], s[20:21]
	v_mov_b64_e32 v[94:95], s[20:21]
	v_mov_b64_e32 v[86:87], s[20:21]
	v_mov_b64_e32 v[78:79], s[20:21]
	v_mov_b64_e32 v[70:71], s[20:21]
	v_mov_b64_e32 v[62:63], s[20:21]
	v_mov_b64_e32 v[54:55], s[20:21]
	v_mov_b64_e32 v[46:47], s[20:21]
	v_mov_b32_e32 v168, 0x79
	v_mov_b32_e32 v169, 0x7f
	s_addc_u32 s27, s42, s1
	s_add_i32 s33, s8, 0
	s_load_dwordx2 s[12:13], s[12:13], 0xd0
	s_add_i32 s43, s33, 0x10000
	s_mov_b32 s0, m0
	s_mov_b32 m0, s43
	s_nop 3
	global_load_lds_dwordx4 v165, s[26:27]
	s_mov_b32 m0, s0
	s_add_i32 s44, s33, 0x12000
	s_mov_b32 s0, m0
	s_mov_b32 m0, s44
	s_nop 3
	global_load_lds_dwordx4 v167, s[26:27]
	s_mov_b32 m0, s0
	s_add_u32 s0, s26, 0x20000
	s_addc_u32 s1, s27, 0
	s_add_i32 s45, s33, 0x14000
	s_mov_b32 s8, m0
	s_mov_b32 m0, s45
	s_nop 3
	global_load_lds_dwordx4 v165, s[0:1]
	s_mov_b32 m0, s8
	s_add_i32 s47, s33, 0x16000
	s_mov_b32 s8, m0
	s_mov_b32 m0, s47
	s_nop 3
	global_load_lds_dwordx4 v167, s[0:1]
	s_mov_b32 m0, s8
	s_mov_b32 s34, s39
	s_mov_b32 s35, s40
	v_readlane_b32 s36, v252, 13
	s_lshl_b32 s36, s36, 10
	s_add_u32 s36, s39, s36
	s_addc_u32 s37, s40, 0
	s_add_u32 s36, s36, 0x18c00000
	s_addc_u32 s37, s37, 0
	global_load_dword v238, v236, s[36:37]
	global_load_dword v239, v237, s[36:37]
	global_load_dword v240, v236, s[36:37] offset:512
	global_load_dword v241, v237, s[36:37] offset:512
	s_waitcnt vmcnt(0)
	v_lshl_or_b32 v164, v238, 10, v234
	v_lshl_or_b32 v166, v239, 10, v235
	v_lshl_or_b32 v232, v240, 10, v234
	v_lshl_or_b32 v233, v241, 10, v235
	s_mov_b32 s0, m0
	s_mov_b32 m0, s33
	s_nop 3
	global_load_lds_dwordx4 v164, s[34:35]
	s_mov_b32 m0, s0
	s_add_i32 s48, s33, 0x2000
	s_mov_b32 s0, m0
	s_mov_b32 m0, s48
	s_nop 3
	global_load_lds_dwordx4 v166, s[34:35]
	s_mov_b32 m0, s0
	s_add_u32 s0, s34, 0
	s_addc_u32 s1, s35, 0
	s_add_i32 s49, s33, 0x4000
	s_mov_b32 s8, m0
	s_mov_b32 m0, s49
	s_nop 3
	global_load_lds_dwordx4 v232, s[0:1]
	s_mov_b32 m0, s8
	s_add_i32 s50, s33, 0x6000
	s_mov_b32 s8, m0
	s_mov_b32 m0, s50
	s_nop 3
	global_load_lds_dwordx4 v233, s[0:1]
	s_mov_b32 m0, s8
	s_cmp_eq_u32 s16, 1
	s_cselect_b64 s[0:1], -1, 0
	s_cmp_lg_u32 s16, 1
	s_cbranch_scc1 .LBB0_1220
	s_barrier

.LBB0_1225:
	s_ashr_i32 s17, s16, 31
	s_mov_b64 s[18:19], 0
	s_add_u32 s18, s39, s18
	s_addc_u32 s19, s40, s19
	s_and_b64 s[20:21], s[22:23], exec
	s_cselect_b32 s14, s19, s35
	s_cselect_b32 s17, s18, s34
	s_cselect_b32 s36, s16, s25
	s_lshl_b32 s36, s36, 10
	s_add_u32 s36, s39, s36
	s_addc_u32 s37, s40, 0
	s_add_u32 s36, s36, 0x18c00000
	s_addc_u32 s37, s37, 0
	global_load_dword v238, v236, s[36:37]
	global_load_dword v239, v237, s[36:37]
	global_load_dword v240, v236, s[36:37] offset:512
	global_load_dword v241, v237, s[36:37] offset:512
	s_ashr_i32 s13, s12, 31
	s_lshl_b64 s[20:21], s[12:13], 18
	s_add_u32 s20, s41, s20
	s_addc_u32 s21, s42, s21
	s_and_b64 s[28:29], s[22:23], exec
	s_cselect_b32 s13, s21, s27
	s_cselect_b32 s61, s20, s26
	s_add_u32 s62, s26, 0x100
	s_addc_u32 s63, s27, 0
	s_mov_b32 s64, -2
.LBB0_1226:
	v_add_u32_e32 v2, 0x10000, v171
	v_add_u32_e32 v6, 0x14000, v171
	ds_read_b128 v[26:29], v2
	ds_read_b128 v[30:33], v2 offset:1024
	ds_read_b128 v[18:21], v2 offset:2048
	ds_read_b128 v[22:25], v2 offset:3072
	ds_read_b128 v[10:13], v6
	ds_read_b128 v[14:17], v6 offset:1024
	ds_read_b128 v[2:5], v6 offset:2048
	ds_read_b128 v[6:9], v6 offset:3072
	s_add_u32 s26, s34, 0x100
	s_addc_u32 s27, s35, 0
	s_cmp_eq_u32 s64, 4
	s_cselect_b32 s36, s17, s26
	s_cselect_b32 s37, s14, s27
	s_cselect_b32 s30, s61, s62
	s_cselect_b32 s31, s13, s63
	s_add_u32 s28, s36, 0x80
	s_addc_u32 s29, s37, 0
	ds_read_b128 v[174:177], v172
	ds_read_b128 v[178:181], v172 offset:1024
	ds_read_b128 v[182:185], v172 offset:2048
	ds_read_b128 v[186:189], v172 offset:3072
	ds_read_b128 v[190:193], v172 offset:4096
	ds_read_b128 v[194:197], v172 offset:5120
	ds_read_b128 v[198:201], v172 offset:6144
	ds_read_b128 v[202:205], v172 offset:7168
	s_add_u32 s34, s34, 0x80
	s_addc_u32 s35, s35, 0
	s_mov_b32 s65, m0
	s_mov_b32 m0, s59
	s_nop 3
	global_load_lds_dwordx4 v232, s[34:35]
	s_mov_b32 m0, s65
	s_add_i32 s65, s33, 0xe000
	s_mov_b32 s66, m0
	s_mov_b32 m0, s65
	s_nop 3
	global_load_lds_dwordx4 v233, s[34:35]
	s_mov_b32 m0, s66
	s_waitcnt vmcnt(8)
	s_waitcnt lgkmcnt(0)
	s_barrier
	s_setprio 1
	s_waitcnt lgkmcnt(6)
	v_mfma_scale_f32_16x16x128_f8f6f4 v[154:157], v[26:33], v[174:181], v[154:157], v168, v169 op_sel_hi:[0,0,0]
	v_mfma_scale_f32_16x16x128_f8f6f4 v[146:149], v[18:25], v[174:181], v[146:149], v168, v169 op_sel_hi:[0,0,0]
	s_waitcnt lgkmcnt(4)
	v_mfma_scale_f32_16x16x128_f8f6f4 v[138:141], v[26:33], v[182:189], v[138:141], v168, v169 op_sel_hi:[0,0,0]
	v_mfma_scale_f32_16x16x128_f8f6f4 v[130:133], v[18:25], v[182:189], v[130:133], v168, v169 op_sel_hi:[0,0,0]
	s_waitcnt lgkmcnt(2)
	v_mfma_scale_f32_16x16x128_f8f6f4 v[122:125], v[26:33], v[190:197], v[122:125], v168, v169 op_sel_hi:[0,0,0]
	v_mfma_scale_f32_16x16x128_f8f6f4 v[114:117], v[18:25], v[190:197], v[114:117], v168, v169 op_sel_hi:[0,0,0]
	s_waitcnt lgkmcnt(0)
	v_mfma_scale_f32_16x16x128_f8f6f4 v[106:109], v[26:33], v[198:205], v[106:109], v168, v169 op_sel_hi:[0,0,0]
	v_mfma_scale_f32_16x16x128_f8f6f4 v[98:101], v[18:25], v[198:205], v[98:101], v168, v169 op_sel_hi:[0,0,0]
	s_setprio 0
	s_setprio 1
	v_mfma_scale_f32_16x16x128_f8f6f4 v[158:161], v[10:17], v[174:181], v[158:161], v168, v169 op_sel_hi:[0,0,0]
	v_mfma_scale_f32_16x16x128_f8f6f4 v[150:153], v[2:9], v[174:181], v[150:153], v168, v169 op_sel_hi:[0,0,0]
	v_mfma_scale_f32_16x16x128_f8f6f4 v[142:145], v[10:17], v[182:189], v[142:145], v168, v169 op_sel_hi:[0,0,0]
	v_mfma_scale_f32_16x16x128_f8f6f4 v[134:137], v[2:9], v[182:189], v[134:137], v168, v169 op_sel_hi:[0,0,0]
	v_mfma_scale_f32_16x16x128_f8f6f4 v[126:129], v[10:17], v[190:197], v[126:129], v168, v169 op_sel_hi:[0,0,0]
	v_mfma_scale_f32_16x16x128_f8f6f4 v[118:121], v[2:9], v[190:197], v[118:121], v168, v169 op_sel_hi:[0,0,0]
	v_mfma_scale_f32_16x16x128_f8f6f4 v[110:113], v[10:17], v[198:205], v[110:113], v168, v169 op_sel_hi:[0,0,0]
	v_mfma_scale_f32_16x16x128_f8f6f4 v[102:105], v[2:9], v[198:205], v[102:105], v168, v169 op_sel_hi:[0,0,0]
	s_setprio 0
	s_barrier
	ds_read_b128 v[174:177], v172 offset:16384
	ds_read_b128 v[178:181], v172 offset:17408
	ds_read_b128 v[182:185], v172 offset:18432
	ds_read_b128 v[186:189], v172 offset:19456
	ds_read_b128 v[190:193], v172 offset:20480
	ds_read_b128 v[194:197], v172 offset:21504
	ds_read_b128 v[198:201], v172 offset:22528
	ds_read_b128 v[202:205], v172 offset:23552
	s_mov_b32 s34, m0
	s_mov_b32 m0, s43
	s_nop 3
	global_load_lds_dwordx4 v165, s[30:31]
	s_mov_b32 m0, s34
	s_nop 0
	s_mov_b32 s34, m0
	s_mov_b32 m0, s44
	s_nop 3
	global_load_lds_dwordx4 v167, s[30:31]
	s_mov_b32 m0, s34
	s_add_u32 s34, s30, 0x20000
	s_addc_u32 s35, s31, 0
	s_mov_b32 s65, m0
	s_mov_b32 m0, s45
	s_nop 3
	global_load_lds_dwordx4 v165, s[34:35]
	s_mov_b32 m0, s65
	s_nop 0
	s_mov_b32 s65, m0
	s_mov_b32 m0, s47
	s_nop 3
	global_load_lds_dwordx4 v167, s[34:35]
	s_mov_b32 m0, s65
	s_cmp_lg_u32 s64, 4
	s_cbranch_scc1 .Lp8_noswap
	v_lshl_or_b32 v164, v238, 10, v234
	v_lshl_or_b32 v166, v239, 10, v235
	v_lshl_or_b32 v232, v240, 10, v234
	v_lshl_or_b32 v233, v241, 10, v235
.Lp8_noswap:
	s_mov_b32 s34, m0
	s_mov_b32 m0, s33
	s_nop 3
	global_load_lds_dwordx4 v164, s[36:37]
	s_mov_b32 m0, s34
	s_nop 0
	s_mov_b32 s34, m0
	s_mov_b32 m0, s48
	s_nop 3
	global_load_lds_dwordx4 v166, s[36:37]
	s_mov_b32 m0, s34
	s_waitcnt vmcnt(8)
	s_waitcnt lgkmcnt(0)
	s_barrier
	s_setprio 1
	s_waitcnt lgkmcnt(6)
	v_mfma_scale_f32_16x16x128_f8f6f4 v[90:93], v[26:33], v[174:181], v[90:93], v168, v169 op_sel_hi:[0,0,0]
	v_mfma_scale_f32_16x16x128_f8f6f4 v[82:85], v[18:25], v[174:181], v[82:85], v168, v169 op_sel_hi:[0,0,0]
	s_waitcnt lgkmcnt(4)
	v_mfma_scale_f32_16x16x128_f8f6f4 v[74:77], v[26:33], v[182:189], v[74:77], v168, v169 op_sel_hi:[0,0,0]
	v_mfma_scale_f32_16x16x128_f8f6f4 v[66:69], v[18:25], v[182:189], v[66:69], v168, v169 op_sel_hi:[0,0,0]
	s_waitcnt lgkmcnt(2)
	v_mfma_scale_f32_16x16x128_f8f6f4 v[58:61], v[26:33], v[190:197], v[58:61], v168, v169 op_sel_hi:[0,0,0]
	v_mfma_scale_f32_16x16x128_f8f6f4 v[50:53], v[18:25], v[190:197], v[50:53], v168, v169 op_sel_hi:[0,0,0]
	s_waitcnt lgkmcnt(0)
	v_mfma_scale_f32_16x16x128_f8f6f4 v[42:45], v[26:33], v[198:205], v[42:45], v168, v169 op_sel_hi:[0,0,0]
	v_mfma_scale_f32_16x16x128_f8f6f4 v[38:41], v[18:25], v[198:205], v[38:41], v168, v169 op_sel_hi:[0,0,0]
	s_setprio 0
	s_setprio 1
	v_mfma_scale_f32_16x16x128_f8f6f4 v[94:97], v[10:17], v[174:181], v[94:97], v168, v169 op_sel_hi:[0,0,0]
	v_mfma_scale_f32_16x16x128_f8f6f4 v[86:89], v[2:9], v[174:181], v[86:89], v168, v169 op_sel_hi:[0,0,0]
	v_mfma_scale_f32_16x16x128_f8f6f4 v[78:81], v[10:17], v[182:189], v[78:81], v168, v169 op_sel_hi:[0,0,0]
	v_mfma_scale_f32_16x16x128_f8f6f4 v[70:73], v[2:9], v[182:189], v[70:73], v168, v169 op_sel_hi:[0,0,0]
	v_mfma_scale_f32_16x16x128_f8f6f4 v[62:65], v[10:17], v[190:197], v[62:65], v168, v169 op_sel_hi:[0,0,0]
	v_mfma_scale_f32_16x16x128_f8f6f4 v[54:57], v[2:9], v[190:197], v[54:57], v168, v169 op_sel_hi:[0,0,0]
	v_mfma_scale_f32_16x16x128_f8f6f4 v[46:49], v[10:17], v[198:205], v[46:49], v168, v169 op_sel_hi:[0,0,0]
	v_mfma_scale_f32_16x16x128_f8f6f4 v[34:37], v[2:9], v[198:205], v[34:37], v168, v169 op_sel_hi:[0,0,0]
	s_setprio 0
	s_barrier
	v_add_u32_e32 v2, 0x18000, v171
	v_add_u32_e32 v6, 0x1c000, v171
	ds_read_b128 v[26:29], v2
	ds_read_b128 v[30:33], v2 offset:1024
	ds_read_b128 v[18:21], v2 offset:2048
	ds_read_b128 v[22:25], v2 offset:3072
	ds_read_b128 v[10:13], v6
	ds_read_b128 v[14:17], v6 offset:1024
	ds_read_b128 v[2:5], v6 offset:2048
	ds_read_b128 v[6:9], v6 offset:3072
	ds_read_b128 v[174:177], v172 offset:32768
	ds_read_b128 v[178:181], v172 offset:33792
	ds_read_b128 v[182:185], v172 offset:34816
	ds_read_b128 v[186:189], v172 offset:35840
	ds_read_b128 v[190:193], v172 offset:36864
	ds_read_b128 v[194:197], v172 offset:37888
	ds_read_b128 v[198:201], v172 offset:38912
	ds_read_b128 v[202:205], v172 offset:39936
	s_add_u32 s34, s36, 0
	s_addc_u32 s35, s37, 0
	s_mov_b32 s36, m0
	s_mov_b32 m0, s49
	s_nop 3
	global_load_lds_dwordx4 v232, s[34:35]
	s_mov_b32 m0, s36
	s_nop 0
	s_mov_b32 s36, m0
	s_mov_b32 m0, s50
	s_nop 3
	global_load_lds_dwordx4 v233, s[34:35]
	s_mov_b32 m0, s36
	s_waitcnt vmcnt(8)
	s_waitcnt lgkmcnt(0)
	s_barrier
	s_setprio 1
	s_waitcnt lgkmcnt(6)
	v_mfma_scale_f32_16x16x128_f8f6f4 v[154:157], v[26:33], v[174:181], v[154:157], v168, v169 op_sel_hi:[0,0,0]
	v_mfma_scale_f32_16x16x128_f8f6f4 v[146:149], v[18:25], v[174:181], v[146:149], v168, v169 op_sel_hi:[0,0,0]
	s_waitcnt lgkmcnt(4)
	v_mfma_scale_f32_16x16x128_f8f6f4 v[138:141], v[26:33], v[182:189], v[138:141], v168, v169 op_sel_hi:[0,0,0]
	v_mfma_scale_f32_16x16x128_f8f6f4 v[130:133], v[18:25], v[182:189], v[130:133], v168, v169 op_sel_hi:[0,0,0]
	s_waitcnt lgkmcnt(2)
	v_mfma_scale_f32_16x16x128_f8f6f4 v[122:125], v[26:33], v[190:197], v[122:125], v168, v169 op_sel_hi:[0,0,0]
	v_mfma_scale_f32_16x16x128_f8f6f4 v[114:117], v[18:25], v[190:197], v[114:117], v168, v169 op_sel_hi:[0,0,0]
	s_waitcnt lgkmcnt(0)
	v_mfma_scale_f32_16x16x128_f8f6f4 v[106:109], v[26:33], v[198:205], v[106:109], v168, v169 op_sel_hi:[0,0,0]
	v_mfma_scale_f32_16x16x128_f8f6f4 v[98:101], v[18:25], v[198:205], v[98:101], v168, v169 op_sel_hi:[0,0,0]
	s_setprio 0
	s_setprio 1
	v_mfma_scale_f32_16x16x128_f8f6f4 v[158:161], v[10:17], v[174:181], v[158:161], v168, v169 op_sel_hi:[0,0,0]
	v_mfma_scale_f32_16x16x128_f8f6f4 v[150:153], v[2:9], v[174:181], v[150:153], v168, v169 op_sel_hi:[0,0,0]
	v_mfma_scale_f32_16x16x128_f8f6f4 v[142:145], v[10:17], v[182:189], v[142:145], v168, v169 op_sel_hi:[0,0,0]
	v_mfma_scale_f32_16x16x128_f8f6f4 v[134:137], v[2:9], v[182:189], v[134:137], v168, v169 op_sel_hi:[0,0,0]
	v_mfma_scale_f32_16x16x128_f8f6f4 v[126:129], v[10:17], v[190:197], v[126:129], v168, v169 op_sel_hi:[0,0,0]
	v_mfma_scale_f32_16x16x128_f8f6f4 v[118:121], v[2:9], v[190:197], v[118:121], v168, v169 op_sel_hi:[0,0,0]
	v_mfma_scale_f32_16x16x128_f8f6f4 v[110:113], v[10:17], v[198:205], v[110:113], v168, v169 op_sel_hi:[0,0,0]
	v_mfma_scale_f32_16x16x128_f8f6f4 v[102:105], v[2:9], v[198:205], v[102:105], v168, v169 op_sel_hi:[0,0,0]
	s_setprio 0
	s_barrier
	ds_read_b128 v[174:177], v172 offset:49152
	ds_read_b128 v[178:181], v172 offset:50176
	ds_read_b128 v[182:185], v172 offset:51200
	ds_read_b128 v[186:189], v172 offset:52224
	ds_read_b128 v[190:193], v172 offset:53248
	ds_read_b128 v[194:197], v172 offset:54272
	ds_read_b128 v[198:201], v172 offset:55296
	ds_read_b128 v[202:205], v172 offset:56320
	s_add_u32 s34, s30, 0x80
	s_addc_u32 s35, s31, 0
	s_mov_b32 s36, m0
	s_mov_b32 m0, s53
	s_nop 3
	global_load_lds_dwordx4 v165, s[34:35]
	s_mov_b32 m0, s36
	s_add_u32 s30, s30, 0x20080
	s_mov_b32 s36, m0
	s_mov_b32 m0, s54
	s_nop 3
	global_load_lds_dwordx4 v167, s[34:35]
	s_mov_b32 m0, s36
	s_addc_u32 s31, s31, 0
	s_mov_b32 s34, m0
	s_mov_b32 m0, s57
	s_nop 3
	global_load_lds_dwordx4 v165, s[30:31]
	s_mov_b32 m0, s34
	s_nop 0
	s_mov_b32 s34, m0
	s_mov_b32 m0, s58
	s_nop 3
	global_load_lds_dwordx4 v167, s[30:31]
	s_mov_b32 m0, s34
	s_mov_b32 s30, m0
	s_mov_b32 m0, s55
	s_nop 3
	global_load_lds_dwordx4 v164, s[28:29]
	s_mov_b32 m0, s30
	s_nop 0
	s_mov_b32 s30, m0
	s_mov_b32 m0, s56
	s_nop 3
	global_load_lds_dwordx4 v166, s[28:29]
	s_mov_b32 m0, s30
	s_waitcnt vmcnt(8)
	s_waitcnt lgkmcnt(0)
	s_barrier
	s_setprio 1
	s_waitcnt lgkmcnt(6)
	v_mfma_scale_f32_16x16x128_f8f6f4 v[90:93], v[26:33], v[174:181], v[90:93], v168, v169 op_sel_hi:[0,0,0]
	v_mfma_scale_f32_16x16x128_f8f6f4 v[82:85], v[18:25], v[174:181], v[82:85], v168, v169 op_sel_hi:[0,0,0]
	s_waitcnt lgkmcnt(4)
	v_mfma_scale_f32_16x16x128_f8f6f4 v[74:77], v[26:33], v[182:189], v[74:77], v168, v169 op_sel_hi:[0,0,0]
	v_mfma_scale_f32_16x16x128_f8f6f4 v[66:69], v[18:25], v[182:189], v[66:69], v168, v169 op_sel_hi:[0,0,0]
	s_waitcnt lgkmcnt(2)
	v_mfma_scale_f32_16x16x128_f8f6f4 v[58:61], v[26:33], v[190:197], v[58:61], v168, v169 op_sel_hi:[0,0,0]
	v_mfma_scale_f32_16x16x128_f8f6f4 v[50:53], v[18:25], v[190:197], v[50:53], v168, v169 op_sel_hi:[0,0,0]
	s_waitcnt lgkmcnt(0)
	v_mfma_scale_f32_16x16x128_f8f6f4 v[42:45], v[26:33], v[198:205], v[42:45], v168, v169 op_sel_hi:[0,0,0]
	v_mfma_scale_f32_16x16x128_f8f6f4 v[38:41], v[18:25], v[198:205], v[38:41], v168, v169 op_sel_hi:[0,0,0]
	s_setprio 0
	s_setprio 1
	v_mfma_scale_f32_16x16x128_f8f6f4 v[94:97], v[10:17], v[174:181], v[94:97], v168, v169 op_sel_hi:[0,0,0]
	v_mfma_scale_f32_16x16x128_f8f6f4 v[86:89], v[2:9], v[174:181], v[86:89], v168, v169 op_sel_hi:[0,0,0]
	v_mfma_scale_f32_16x16x128_f8f6f4 v[78:81], v[10:17], v[182:189], v[78:81], v168, v169 op_sel_hi:[0,0,0]
	v_mfma_scale_f32_16x16x128_f8f6f4 v[70:73], v[2:9], v[182:189], v[70:73], v168, v169 op_sel_hi:[0,0,0]
	v_mfma_scale_f32_16x16x128_f8f6f4 v[62:65], v[10:17], v[190:197], v[62:65], v168, v169 op_sel_hi:[0,0,0]
	v_mfma_scale_f32_16x16x128_f8f6f4 v[54:57], v[2:9], v[190:197], v[54:57], v168, v169 op_sel_hi:[0,0,0]
	v_mfma_scale_f32_16x16x128_f8f6f4 v[46:49], v[10:17], v[198:205], v[46:49], v168, v169 op_sel_hi:[0,0,0]
	v_mfma_scale_f32_16x16x128_f8f6f4 v[34:37], v[2:9], v[198:205], v[34:37], v168, v169 op_sel_hi:[0,0,0]
	s_setprio 0
	s_barrier
	s_add_i32 s64, s64, 2
	s_add_u32 s62, s62, 0x100
	s_addc_u32 s63, s63, 0
	s_cmp_gt_u32 s64, 5
	s_mov_b64 s[34:35], s[26:27]
	s_cbranch_scc0 .LBB0_1226
	s_and_b64 vcc, exec, s[10:11]
	s_cbranch_vccz .LBB0_1229
	s_barrier
